# v7: ph4 conv loads issued back-to-back (d16_hi), ph12 epilogue SWE loads hoisted, ph6 unit-tail gate/gain loads hoisted before the barrier
# speedup vs baseline: 1.0025x; 1.0025x over previous
; __device__ __forceinline__ void ph4_unit(const Frame& F, const Args& A, int c, int h) {
;     ...
;     float zin[19];
; #pragma unroll
;     for (int i = 0; i < 19; ++i) { const int tt = tb - 3 + i; zin[i] = tt >= 0 ? pg8::bf2f(Z[(size_t)tt * pg8::ZLD + zc]) : 0.f; }
.LBB0_334:
	s_ashr_i32 s59, s58, 3
	s_and_b32 s50, s58, 7
	s_lshl_b32 s49, s59, 6
	v_lshl_or_b32 v76, s50, 6, v91
	v_add_u32_e32 v10, s49, v84
	v_lshlrev_b32_e32 v18, 1, v76
	v_lshl_add_u64 v[2:3], s[28:29], 0, v[18:19]
	v_cmp_lt_i32_e32 vcc, 2, v10
	v_mov_b32_e32 v11, 0
	s_and_saveexec_b64 s[0:1], vcc
	s_cbranch_execz .LBB0_336
	v_add_u32_e32 v4, -3, v10
	v_mad_u64_u32 v[4:5], s[60:61], v4, s55, v[2:3]
	global_load_short_d16_hi v11, v[4:5], off
.LBB0_336:
	s_or_b64 exec, exec, s[0:1]
	v_cmp_lt_i32_e32 vcc, 1, v10
	v_mov_b32_e32 v111, 0
	v_mov_b32_e32 v112, 0
	s_and_saveexec_b64 s[0:1], vcc
	s_cbranch_execz .LBB0_338
	v_add_u32_e32 v4, -2, v10
	v_mad_u64_u32 v[4:5], s[60:61], v4, s55, v[2:3]
	global_load_short_d16_hi v112, v[4:5], off
.LBB0_338:
	s_or_b64 exec, exec, s[0:1]
	v_cmp_lt_i32_e32 vcc, 0, v10
	s_and_saveexec_b64 s[0:1], vcc
	s_cbranch_execz .LBB0_340
	v_add_u32_e32 v4, -1, v10
	v_mad_u64_u32 v[4:5], s[60:61], v4, s55, v[2:3]
	global_load_short_d16_hi v111, v[4:5], off
.LBB0_340:
	s_or_b64 exec, exec, s[0:1]
	v_cmp_lt_i32_e32 vcc, -1, v10
	v_mov_b32_e32 v109, 0
	v_mov_b32_e32 v110, 0
	s_and_saveexec_b64 s[0:1], vcc
	s_cbranch_execz .LBB0_342
	v_mad_u64_u32 v[4:5], s[60:61], v10, s55, v[2:3]
	global_load_short_d16_hi v110, v[4:5], off
.LBB0_342:
	s_or_b64 exec, exec, s[0:1]
	s_and_saveexec_b64 s[0:1], vcc
	s_cbranch_execz .LBB0_344
	v_or_b32_e32 v4, 1, v10
	v_mad_u64_u32 v[4:5], s[60:61], v4, s55, v[2:3]
	global_load_short_d16_hi v109, v[4:5], off
.LBB0_344:
	s_or_b64 exec, exec, s[0:1]
	v_mov_b32_e32 v83, 0
	v_mov_b32_e32 v108, 0
	s_and_saveexec_b64 s[0:1], vcc
	s_cbranch_execz .LBB0_346
	v_or_b32_e32 v4, 2, v10
	v_mad_u64_u32 v[4:5], s[60:61], v4, s55, v[2:3]
	global_load_short_d16_hi v108, v[4:5], off
.LBB0_346:
	s_or_b64 exec, exec, s[0:1]
	s_and_saveexec_b64 s[0:1], vcc
	s_cbranch_execz .LBB0_348
	v_or_b32_e32 v4, 3, v10
	v_mad_u64_u32 v[4:5], s[60:61], v4, s55, v[2:3]
	global_load_short_d16_hi v83, v[4:5], off
.LBB0_348:
	s_or_b64 exec, exec, s[0:1]
	v_mov_b32_e32 v73, 0
	v_mov_b32_e32 v79, 0
	s_and_saveexec_b64 s[0:1], vcc
	s_cbranch_execz .LBB0_350
	v_or_b32_e32 v4, 4, v10
	v_mad_u64_u32 v[4:5], s[60:61], v4, s55, v[2:3]
	global_load_short_d16_hi v79, v[4:5], off
.LBB0_350:
	s_or_b64 exec, exec, s[0:1]
	s_and_saveexec_b64 s[0:1], vcc
	s_cbranch_execz .LBB0_352
	v_or_b32_e32 v4, 5, v10
	v_mad_u64_u32 v[4:5], s[60:61], v4, s55, v[2:3]
	global_load_short_d16_hi v73, v[4:5], off
.LBB0_352:
	s_or_b64 exec, exec, s[0:1]
	v_mov_b32_e32 v71, 0
	v_mov_b32_e32 v72, 0
	s_and_saveexec_b64 s[0:1], vcc
	s_cbranch_execz .LBB0_354
	v_or_b32_e32 v4, 6, v10
	v_mad_u64_u32 v[4:5], s[60:61], v4, s55, v[2:3]
	global_load_short_d16_hi v72, v[4:5], off
.LBB0_354:
	s_or_b64 exec, exec, s[0:1]
	s_and_saveexec_b64 s[0:1], vcc
	s_cbranch_execz .LBB0_356
	v_or_b32_e32 v4, 7, v10
	v_mad_u64_u32 v[4:5], s[60:61], v4, s55, v[2:3]
	global_load_short_d16_hi v71, v[4:5], off
.LBB0_356:
	s_or_b64 exec, exec, s[0:1]
	v_mov_b32_e32 v68, 0
	v_mov_b32_e32 v70, 0
	s_and_saveexec_b64 s[0:1], vcc
	s_cbranch_execz .LBB0_358
	v_or_b32_e32 v4, 8, v10
	v_mad_u64_u32 v[4:5], s[60:61], v4, s55, v[2:3]
	global_load_short_d16_hi v70, v[4:5], off
.LBB0_358:
	s_or_b64 exec, exec, s[0:1]
	s_and_saveexec_b64 s[0:1], vcc
	s_cbranch_execz .LBB0_360
	v_or_b32_e32 v4, 9, v10
	v_mad_u64_u32 v[4:5], s[60:61], v4, s55, v[2:3]
	global_load_short_d16_hi v68, v[4:5], off
.LBB0_360:
	s_or_b64 exec, exec, s[0:1]
	v_mov_b32_e32 v15, 0
	v_mov_b32_e32 v17, 0
	s_and_saveexec_b64 s[0:1], vcc
	s_cbranch_execz .LBB0_362
	v_or_b32_e32 v4, 10, v10
	v_mad_u64_u32 v[4:5], s[60:61], v4, s55, v[2:3]
	global_load_short_d16_hi v17, v[4:5], off
.LBB0_362:
	s_or_b64 exec, exec, s[0:1]
	s_and_saveexec_b64 s[0:1], vcc
	s_cbranch_execz .LBB0_364
	v_or_b32_e32 v4, 11, v10
	v_mad_u64_u32 v[4:5], s[60:61], v4, s55, v[2:3]
	global_load_short_d16_hi v15, v[4:5], off
.LBB0_364:
	s_or_b64 exec, exec, s[0:1]
	v_mov_b32_e32 v12, 0
	v_mov_b32_e32 v13, 0
	s_and_saveexec_b64 s[0:1], vcc
	s_cbranch_execz .LBB0_366
	v_or_b32_e32 v4, 12, v10
	v_mad_u64_u32 v[4:5], s[60:61], v4, s55, v[2:3]
	global_load_short_d16_hi v13, v[4:5], off
.LBB0_366:
	s_or_b64 exec, exec, s[0:1]
	s_and_saveexec_b64 s[0:1], vcc
	s_cbranch_execz .LBB0_368
	v_or_b32_e32 v4, 13, v10
	v_mad_u64_u32 v[4:5], s[60:61], v4, s55, v[2:3]
	global_load_short_d16_hi v12, v[4:5], off
.LBB0_368:
	s_or_b64 exec, exec, s[0:1]
	v_mov_b32_e32 v14, 0
	v_mov_b32_e32 v16, 0
	s_and_saveexec_b64 s[0:1], vcc
	s_cbranch_execz .LBB0_370
	v_or_b32_e32 v4, 14, v10
	v_mad_u64_u32 v[4:5], s[60:61], v4, s55, v[2:3]
	global_load_short_d16_hi v16, v[4:5], off
.LBB0_370:
	s_or_b64 exec, exec, s[0:1]
	s_and_saveexec_b64 s[0:1], vcc
	s_cbranch_execz .LBB0_372
	v_or_b32_e32 v4, 15, v10
	v_mad_u64_u32 v[2:3], s[60:61], v4, s55, v[2:3]
	global_load_short_d16_hi v14, v[2:3], off

; __device__ __forceinline__ unsigned pk2(float lo, float hi) { const f32x2_t v = {lo, hi}; return __builtin_bit_cast(unsigned, __builtin_convertvector(v, bf16x2_hw)); }
; __device__ __forceinline__ float sigm(float x) { return __builtin_amdgcn_rcpf(1.f + __builtin_amdgcn_exp2f(-1.4426950408889634f * x)); }
; __device__ __forceinline__ void ph6_unit(const Frame& F, const Args& A, int c, int h) {
;     ...
;     ss += __shfl_xor(ss, 32);
;     if (hi == 0) ssq[eb * 64 + t] = ss;
;     __syncthreads();
;     const float r = 1.f / sqrtf((ssq[t] + ssq[64 + t] + ssq[128 + t] + ssq[192 + t]) * (1.f / 128.f) + EPS_);
;     const float* mg = A.in[I_MONG] + h * 128 + 32 * eb + 4 * hi;
;     const unsigned char* og = ws + WS_Z8 + (size_t)(t0 + t) * pg8::Z8LD + h * 128 + 32 * eb + 4 * hi;
;     bf16* hm = (bf16*)(ws + WS_HMF) + (size_t)(t0 + t) * 2048 + h * 128 + 32 * eb + 4 * hi;
; #pragma unroll
;     for (int g = 0; g < 4; ++g) { const unsigned ow = *(const unsigned*)(og + 8 * g); const f32x4 gm = *(const f32x4*)(mg + 8 * g);
;         const auto o01 = __builtin_amdgcn_cvt_pk_f32_fp8((int)ow, false), o23 = __builtin_amdgcn_cvt_pk_f32_fp8((int)ow, true);
;         uint2 pw; pw.x = pk2(o[4 * g] * r * gm.x * sigm(o01[0]), o[4 * g + 1] * r * gm.y * sigm(o01[1]));
;         pw.y = pk2(o[4 * g + 2] * r * gm.z * sigm(o23[0]), o[4 * g + 3] * r * gm.w * sigm(o23[1]));
;         *(uint2*)(hm + 8 * g) = pw; }
;     __syncthreads();
.LBB0_941:
	s_or_b64 exec, exec, s[50:51]
	v_or_b32_e32 v22, s0, v67
	s_waitcnt lgkmcnt(0)
	v_mov_b64_e32 v[10:11], s[56:57]
	s_movk_i32 s0, 0x1800
	v_mad_i64_i32 v[10:11], s[0:1], v22, s0, v[10:11]
	v_lshl_add_u64 v[10:11], v[10:11], 0, s[96:97]
	v_lshl_add_u64 v[10:11], v[10:11], 0, s[10:11]
	v_lshl_add_u64 v[10:11], v[10:11], 0, v[50:51]
	s_lshl_b32 s0, s96, 2
	s_mov_b32 s1, s97
	v_lshl_add_u64 v[12:13], v[52:53], 0, s[0:1]
	global_load_dword v30, v[10:11], off
	global_load_dwordx4 v[14:17], v[12:13], off
	global_load_dword v100, v[10:11], off offset:8
	global_load_dwordx4 v[104:107], v[12:13], off offset:32
	global_load_dword v101, v[10:11], off offset:16
	global_load_dwordx4 v[108:111], v[12:13], off offset:64
	global_load_dword v102, v[10:11], off offset:24
	global_load_dwordx4 v[112:115], v[12:13], off offset:96
	s_barrier
	ds_read2st64_b32 v[24:25], v80 offset0:252 offset1:253
	ds_read2st64_b32 v[26:27], v80 offset0:254 offset1:255
	s_mov_b32 s0, 0xf800000
	v_ashrrev_i32_e32 v23, 31, v22
	v_lshlrev_b64 v[22:23], 12, v[22:23]
	s_waitcnt lgkmcnt(1)
	v_add_f32_e32 v24, v24, v25
	s_waitcnt lgkmcnt(0)
	v_add_f32_e32 v24, v24, v26
	v_add_f32_e32 v24, v24, v27
	v_fmamk_f32 v24, v24, 0x3c000000, v77
	v_mul_f32_e32 v25, 0x4f800000, v24
	v_cmp_gt_f32_e32 vcc, s0, v24
	s_lshl_b32 s96, s96, 1
	v_lshl_add_u64 v[22:23], s[72:73], 0, v[22:23]
	v_cndmask_b32_e32 v24, v24, v25, vcc
	v_sqrt_f32_e32 v25, v24
	s_mov_b32 s77, s97
	v_lshl_add_u64 v[22:23], v[22:23], 0, s[96:97]
	v_mov_b32_e32 v55, v47
	v_add_u32_e32 v26, -1, v25
	v_add_u32_e32 v27, 1, v25
	v_fma_f32 v28, -v26, v25, v24
	v_fma_f32 v29, -v27, v25, v24
	v_cmp_ge_f32_e64 s[0:1], 0, v28
	v_lshl_add_u64 v[22:23], v[22:23], 0, s[76:77]
	v_lshl_add_u64 v[22:23], v[22:23], 0, v[54:55]
	v_cndmask_b32_e64 v25, v25, v26, s[0:1]
	v_cmp_lt_f32_e64 s[0:1], 0, v29
	s_add_i32 s89, s89, s92
	s_cmpk_gt_i32 s89, 0x3ff
	v_cndmask_b32_e64 v25, v25, v27, s[0:1]
	v_mul_f32_e32 v26, 0x37800000, v25
	v_cndmask_b32_e32 v25, v25, v26, vcc
	v_cmp_class_f32_e32 vcc, v24, v78
	s_nop 1
	v_cndmask_b32_e32 v24, v25, v24, vcc
	v_div_scale_f32 v25, s[0:1], v24, v24, 1.0
	v_rcp_f32_e32 v26, v25
	v_div_scale_f32 v27, vcc, 1.0, v24, 1.0
	v_fma_f32 v28, -v25, v26, 1.0
	v_fmac_f32_e32 v26, v28, v26
	v_mul_f32_e32 v28, v27, v26
	v_fma_f32 v29, -v25, v28, v27
	v_fmac_f32_e32 v28, v29, v26
	v_fma_f32 v25, -v25, v28, v27
	v_div_fmas_f32 v25, v25, v26, v28
	v_div_fixup_f32 v24, v25, v24, 1.0
	v_pk_mul_f32 v[28:29], v[58:59], v[24:25] op_sel_hi:[1,0]
	v_pk_mul_f32 v[32:33], v[60:61], v[24:25] op_sel_hi:[1,0]
	s_waitcnt vmcnt(0)
	v_cvt_pk_f32_fp8_e32 v[26:27], v30
	v_cvt_pk_f32_fp8_sdwa v[30:31], v30 src0_sel:WORD_1
	v_mul_f32_e32 v25, 0xbfb8aa3b, v26
	v_mul_f32_e32 v26, 0xbfb8aa3b, v27
	v_mul_f32_e32 v27, 0xbfb8aa3b, v30
	v_mul_f32_e32 v30, 0xbfb8aa3b, v31
	v_exp_f32_e32 v25, v25
	v_exp_f32_e32 v26, v26
	v_exp_f32_e32 v27, v27
	v_exp_f32_e32 v30, v30
	v_add_f32_e32 v25, 1.0, v25
	v_add_f32_e32 v31, 1.0, v26
	v_add_f32_e32 v55, 1.0, v27
	v_add_f32_e32 v58, 1.0, v30
	v_rcp_f32_e32 v26, v25
	v_rcp_f32_e32 v27, v31
	v_rcp_f32_e32 v30, v55
	v_rcp_f32_e32 v31, v58
	s_waitcnt vmcnt(0)
	v_pk_mul_f32 v[14:15], v[14:15], v[28:29]
	v_pk_mul_f32 v[16:17], v[16:17], v[32:33]
	v_pk_mul_f32 v[14:15], v[14:15], v[26:27]
	v_pk_mul_f32 v[16:17], v[16:17], v[30:31]
	v_cvt_pk_bf16_f32 v14, v14, v15
	v_cvt_pk_bf16_f32 v15, v16, v17
	global_store_dwordx2 v[22:23], v[14:15], off
	v_mov_b32_e32 v25, v100
	s_nop 1
	v_mov_b64_e32 v[14:15], v[104:105]
	v_mov_b64_e32 v[16:17], v[106:107]
	v_cvt_pk_f32_fp8_e32 v[26:27], v25
	v_cvt_pk_f32_fp8_sdwa v[28:29], v25 src0_sel:WORD_1
	v_pk_mul_f32 v[18:19], v[18:19], v[24:25] op_sel_hi:[1,0]
	v_pk_mul_f32 v[20:21], v[20:21], v[24:25] op_sel_hi:[1,0]
	v_mul_f32_e32 v25, 0xbfb8aa3b, v26
	v_mul_f32_e32 v26, 0xbfb8aa3b, v27
	v_mul_f32_e32 v27, 0xbfb8aa3b, v28
	v_mul_f32_e32 v28, 0xbfb8aa3b, v29
	v_exp_f32_e32 v25, v25
	v_exp_f32_e32 v26, v26
	v_exp_f32_e32 v27, v27
	v_exp_f32_e32 v28, v28
	v_add_f32_e32 v25, 1.0, v25
	v_add_f32_e32 v29, 1.0, v26
	v_add_f32_e32 v30, 1.0, v27
	v_add_f32_e32 v31, 1.0, v28
	v_rcp_f32_e32 v26, v25
	v_rcp_f32_e32 v27, v29
	v_rcp_f32_e32 v28, v30
	v_rcp_f32_e32 v29, v31
	v_pk_mul_f32 v[14:15], v[18:19], v[14:15]
	v_pk_mul_f32 v[16:17], v[20:21], v[16:17]
	v_pk_mul_f32 v[14:15], v[14:15], v[26:27]
	v_pk_mul_f32 v[16:17], v[16:17], v[28:29]
	v_cvt_pk_bf16_f32 v14, v14, v15
	v_cvt_pk_bf16_f32 v15, v16, v17
	global_store_dwordx2 v[22:23], v[14:15], off offset:16
	v_mov_b32_e32 v20, v101
	s_nop 1
	v_mov_b64_e32 v[14:15], v[108:109]
	v_mov_b64_e32 v[16:17], v[110:111]
	v_pk_mul_f32 v[8:9], v[8:9], v[24:25] op_sel_hi:[1,0]
	v_pk_mul_f32 v[6:7], v[6:7], v[24:25] op_sel_hi:[1,0]
	v_pk_mul_f32 v[2:3], v[2:3], v[24:25] op_sel_hi:[1,0]
	v_pk_mul_f32 v[4:5], v[4:5], v[24:25] op_sel_hi:[1,0]
	v_cvt_pk_f32_fp8_e32 v[18:19], v20
	v_cvt_pk_f32_fp8_sdwa v[20:21], v20 src0_sel:WORD_1
	v_pk_mul_f32 v[8:9], v[8:9], v[14:15]
	v_pk_mul_f32 v[6:7], v[6:7], v[16:17]
	v_mul_f32_e32 v18, 0xbfb8aa3b, v18
	v_mul_f32_e32 v19, 0xbfb8aa3b, v19
	v_mul_f32_e32 v20, 0xbfb8aa3b, v20
	v_mul_f32_e32 v21, 0xbfb8aa3b, v21
	v_exp_f32_e32 v18, v18
	v_exp_f32_e32 v19, v19
	v_exp_f32_e32 v20, v20
	v_exp_f32_e32 v21, v21
	v_add_f32_e32 v18, 1.0, v18
	v_add_f32_e32 v19, 1.0, v19
	v_add_f32_e32 v20, 1.0, v20
	v_add_f32_e32 v21, 1.0, v21
	v_rcp_f32_e32 v18, v18
	v_rcp_f32_e32 v19, v19
	v_rcp_f32_e32 v20, v20
	v_rcp_f32_e32 v21, v21
	v_pk_mul_f32 v[8:9], v[8:9], v[18:19]
	s_nop 0
	v_cvt_pk_bf16_f32 v8, v8, v9
	v_pk_mul_f32 v[6:7], v[6:7], v[20:21]
	s_nop 0
	v_cvt_pk_bf16_f32 v9, v6, v7
	global_store_dwordx2 v[22:23], v[8:9], off offset:32
	v_mov_b32_e32 v14, v102
	s_nop 1
	v_mov_b64_e32 v[6:7], v[112:113]
	v_mov_b64_e32 v[8:9], v[114:115]
	v_cvt_pk_f32_fp8_e32 v[10:11], v14
	v_cvt_pk_f32_fp8_sdwa v[12:13], v14 src0_sel:WORD_1
	v_pk_mul_f32 v[2:3], v[2:3], v[6:7]
	v_pk_mul_f32 v[4:5], v[4:5], v[8:9]
	v_mul_f32_e32 v10, 0xbfb8aa3b, v10
	v_mul_f32_e32 v11, 0xbfb8aa3b, v11
	v_mul_f32_e32 v12, 0xbfb8aa3b, v12
	v_mul_f32_e32 v13, 0xbfb8aa3b, v13
	v_exp_f32_e32 v10, v10
	v_exp_f32_e32 v11, v11
	v_exp_f32_e32 v12, v12
	v_exp_f32_e32 v13, v13
	v_add_f32_e32 v10, 1.0, v10
	v_add_f32_e32 v11, 1.0, v11
	v_add_f32_e32 v12, 1.0, v12
	v_add_f32_e32 v13, 1.0, v13
	v_rcp_f32_e32 v10, v10
	v_rcp_f32_e32 v11, v11
	v_rcp_f32_e32 v12, v12
	v_rcp_f32_e32 v13, v13
	v_pk_mul_f32 v[2:3], v[2:3], v[10:11]
	s_nop 0
	v_cvt_pk_bf16_f32 v2, v2, v3
	v_pk_mul_f32 v[4:5], v[4:5], v[12:13]
	s_nop 0
	v_cvt_pk_bf16_f32 v3, v4, v5
	global_store_dwordx2 v[22:23], v[2:3], off offset:48
	s_barrier
	s_cbranch_scc1 .LBB0_968

; __device__ __forceinline__ unsigned pack_fp8x4(float a, float b, float c, float d) { int w = __builtin_amdgcn_cvt_pk_fp8_f32(a, b, 0, false); w = __builtin_amdgcn_cvt_pk_fp8_f32(c, d, w, true); return (unsigned)w; }
;     __device__ __forceinline__ void operator()(const f32x4 (&acc)[2][2][4][2], const Unit& u, int wr, int wc, int fr, int fq) const {
;     ...
;         const int e = u.pn >> 3, j = u.pn & 7, col0 = 256 * j + wc * 32 + 8 * fq, row0 = u.pm * HALF + wr * 64 + fr; const int eoff0 = eoff[e];
;         f32x4 bv[2][2];
; #pragma unroll
;         for (int bj = 0; bj < 2; ++bj)
; #pragma unroll
;             for (int n = 0; n < 2; ++n) bv[bj][n] = *(const f32x4*)(bd + (size_t)e * 2048 + col0 + bj * HALF + 4 * n);
; #pragma unroll
;         for (int ai = 0; ai < 2; ++ai) if (!(ai == 1 && u.half))
; #pragma unroll
;             for (int m = 0; m < 4; ++m) { const size_t row = (size_t)(row0 + ai * HALF + m * 16); const float sw = 32.f * SWE[(size_t)e * 8192 + (row - (size_t)eoff0)];
; #pragma unroll
;                 for (int bj = 0; bj < 2; ++bj) { const f32x4 v0 = (acc[ai][bj][m][0] * 0.015625f + bv[bj][0]) * sw, v1 = (acc[ai][bj][m][1] * 0.015625f + bv[bj][1]) * sw;
;                     uint2 w; w.x = pack_fp8x4(v0[0], v0[1], v0[2], v0[3]); w.y = pack_fp8x4(v1[0], v1[1], v1[2], v1[3]);
;                     *(uint2*)(YS + row * 2048 + col0 + bj * HALF) = w; } }
.LBB0_1475:
	s_ashr_i32 s36, s34, 3
	s_lshl_b32 s23, s36, 2
	s_add_i32 s23, s23, 0
	s_lshl_b32 s21, s34, 8
	s_add_i32 s23, s23, 0x20400
	v_mov_b32_e32 v20, v1
	v_mov_b32_e32 v2, v216
	v_mov_b32_e32 v3, s23
	s_and_b32 s21, s21, 0x700
	s_ashr_i32 s37, s36, 31
	s_nop 15
	s_nop 15
	ds_read_b32 v22, v3
	s_or_b32 s21, s21, s58
	s_lshl_b64 s[38:39], s[36:37], 13
	s_add_u32 s38, s82, s38
	v_lshl_add_u32 v18, v2, 3, s21
	s_addc_u32 s39, s83, s39
	s_lshl_b32 s21, s30, 7
	s_add_i32 s21, s21, s57
	s_lshl_b64 s[36:37], s[36:37], 15
	v_add_u32_e32 v20, s21, v20
	s_waitcnt lgkmcnt(0)
	v_ashrrev_i32_e32 v23, 31, v22
	v_ashrrev_i32_e32 v21, 31, v20
	v_sub_co_u32_e32 v24, vcc, v20, v22
	s_add_u32 s30, s55, s36
	v_ashrrev_i32_e32 v19, 31, v18
	v_subb_co_u32_e32 v25, vcc, v21, v23, vcc
	s_addc_u32 s31, s56, s37
	v_lshl_add_u64 v[6:7], v[18:19], 2, s[38:39]
	v_lshl_add_u64 v[24:25], v[24:25], 2, s[30:31]
	global_load_dwordx4 v[10:13], v[6:7], off offset:16
	global_load_dwordx4 v[14:17], v[6:7], off
	global_load_dwordx4 v[2:5], v[6:7], off offset:528
	s_nop 0
	global_load_dwordx4 v[6:9], v[6:7], off offset:512
	v_mov_b32_e32 v26, 0
	global_load_dword v48, v[24:25], off
	global_load_dword v226, v[24:25], off offset:64
	global_load_dword v227, v[24:25], off offset:128
	global_load_dword v228, v[24:25], off offset:192
	global_load_dword v229, v[24:25], off offset:512
	global_load_dword v230, v[24:25], off offset:576
	global_load_dword v231, v[24:25], off offset:640
	global_load_dword v232, v[24:25], off offset:704
	v_mov_b32_e32 v24, 0
	v_mov_b32_e32 v25, 0
	v_mov_b32_e32 v27, 0
	v_add_u32_e32 v28, 16, v20
	v_lshlrev_b64 v[30:31], 11, v[20:21]
	v_ashrrev_i32_e32 v29, 31, v28
	v_lshl_add_u64 v[30:31], s[6:7], 0, v[30:31]
	v_lshl_add_u64 v[30:31], v[30:31], 0, v[18:19]
	s_waitcnt vmcnt(0)
	v_pk_fma_f32 v[38:39], v[190:191], s[14:15], v[10:11] op_sel_hi:[1,0,1]
	v_pk_fma_f32 v[34:35], v[194:195], s[14:15], v[14:15] op_sel_hi:[1,0,1]
	v_pk_fma_f32 v[46:47], v[182:183], s[14:15], v[2:3] op_sel_hi:[1,0,1]
	v_pk_fma_f32 v[42:43], v[186:187], s[14:15], v[6:7] op_sel_hi:[1,0,1]
	v_pk_fma_f32 v[32:33], v[196:197], s[14:15], v[16:17] op_sel_hi:[1,0,1]
	v_mul_f32_e32 v48, 0x42000000, v48
	v_pk_mul_f32 v[34:35], v[34:35], v[48:49] op_sel_hi:[1,0]
	v_pk_mul_f32 v[38:39], v[38:39], v[48:49] op_sel_hi:[1,0]
	v_pk_mul_f32 v[42:43], v[42:43], v[48:49] op_sel_hi:[1,0]
	v_pk_mul_f32 v[46:47], v[46:47], v[48:49] op_sel_hi:[1,0]
	v_cvt_pk_fp8_f32 v24, v34, v35
	v_cvt_pk_fp8_f32 v25, v38, v39
	v_cvt_pk_fp8_f32 v26, v42, v43
	v_cvt_pk_fp8_f32 v27, v46, v47
	v_pk_fma_f32 v[36:37], v[192:193], s[14:15], v[12:13] op_sel_hi:[1,0,1]
	v_pk_fma_f32 v[40:41], v[188:189], s[14:15], v[8:9] op_sel_hi:[1,0,1]
	v_pk_fma_f32 v[44:45], v[184:185], s[14:15], v[4:5] op_sel_hi:[1,0,1]
	v_pk_mul_f32 v[32:33], v[32:33], v[48:49] op_sel_hi:[1,0]
	v_pk_mul_f32 v[36:37], v[36:37], v[48:49] op_sel_hi:[1,0]
	v_pk_mul_f32 v[40:41], v[40:41], v[48:49] op_sel_hi:[1,0]
	v_pk_mul_f32 v[44:45], v[44:45], v[48:49] op_sel_hi:[1,0]
	v_cvt_pk_fp8_f32 v24, v32, v33 op_sel:[0,0,1]
	v_cvt_pk_fp8_f32 v25, v36, v37 op_sel:[0,0,1]
	v_cvt_pk_fp8_f32 v26, v40, v41 op_sel:[0,0,1]
	v_cvt_pk_fp8_f32 v27, v44, v45 op_sel:[0,0,1]
	v_sub_co_u32_e32 v32, vcc, v28, v22
	global_store_dwordx2 v[30:31], v[24:25], off
	global_store_dwordx2 v[30:31], v[26:27], off offset:128
	v_subb_co_u32_e32 v33, vcc, v29, v23, vcc
	v_lshl_add_u64 v[32:33], v[32:33], 2, s[30:31]
	v_pk_fma_f32 v[36:37], v[178:179], s[14:15], v[14:15] op_sel_hi:[1,0,1]
	v_pk_fma_f32 v[40:41], v[174:175], s[14:15], v[10:11] op_sel_hi:[1,0,1]
	v_mov_b32_e32 v24, 0
	v_mov_b32_e32 v25, 0
	v_pk_fma_f32 v[44:45], v[170:171], s[14:15], v[6:7] op_sel_hi:[1,0,1]
	v_pk_fma_f32 v[48:49], v[166:167], s[14:15], v[2:3] op_sel_hi:[1,0,1]
	v_mov_b32_e32 v26, 0
	v_mov_b32_e32 v27, 0
	v_pk_fma_f32 v[34:35], v[180:181], s[14:15], v[16:17] op_sel_hi:[1,0,1]
	v_pk_fma_f32 v[38:39], v[176:177], s[14:15], v[12:13] op_sel_hi:[1,0,1]
	v_pk_fma_f32 v[42:43], v[172:173], s[14:15], v[8:9] op_sel_hi:[1,0,1]
	v_pk_fma_f32 v[46:47], v[168:169], s[14:15], v[4:5] op_sel_hi:[1,0,1]
	v_add_u32_e32 v30, 32, v20
	v_lshlrev_b64 v[28:29], 11, v[28:29]
	v_ashrrev_i32_e32 v31, 31, v30
	v_lshl_add_u64 v[28:29], s[6:7], 0, v[28:29]
	v_sub_co_u32_e32 v32, vcc, v30, v22
	v_lshl_add_u64 v[28:29], v[28:29], 0, v[18:19]
	s_nop 0
	v_subb_co_u32_e32 v33, vcc, v31, v23, vcc
	v_lshl_add_u64 v[32:33], v[32:33], 2, s[30:31]
	v_lshlrev_b64 v[30:31], 11, v[30:31]
	v_lshl_add_u64 v[30:31], s[6:7], 0, v[30:31]
	v_lshl_add_u64 v[30:31], v[30:31], 0, v[18:19]
	v_mul_f32_e32 v50, 0x42000000, v226
; __device__ __forceinline__ unsigned pack_fp8x4(float a, float b, float c, float d) { int w = __builtin_amdgcn_cvt_pk_fp8_f32(a, b, 0, false); w = __builtin_amdgcn_cvt_pk_fp8_f32(c, d, w, true); return (unsigned)w; }
;     __device__ __forceinline__ void operator()(const f32x4 (&acc)[2][2][4][2], const Unit& u, int wr, int wc, int fr, int fq) const {
;     ...
;             for (int m = 0; m < 4; ++m) { const size_t row = (size_t)(row0 + ai * HALF + m * 16); const float sw = 32.f * SWE[(size_t)e * 8192 + (row - (size_t)eoff0)];
; #pragma unroll
;                 for (int bj = 0; bj < 2; ++bj) { const f32x4 v0 = (acc[ai][bj][m][0] * 0.015625f + bv[bj][0]) * sw, v1 = (acc[ai][bj][m][1] * 0.015625f + bv[bj][1]) * sw;
;                     uint2 w; w.x = pack_fp8x4(v0[0], v0[1], v0[2], v0[3]); w.y = pack_fp8x4(v1[0], v1[1], v1[2], v1[3]);
;                     *(uint2*)(YS + row * 2048 + col0 + bj * HALF) = w; } }
	v_pk_mul_f32 v[36:37], v[36:37], v[50:51] op_sel_hi:[1,0]
	v_pk_mul_f32 v[40:41], v[40:41], v[50:51] op_sel_hi:[1,0]
	v_pk_mul_f32 v[44:45], v[44:45], v[50:51] op_sel_hi:[1,0]
	v_pk_mul_f32 v[48:49], v[48:49], v[50:51] op_sel_hi:[1,0]
	v_cvt_pk_fp8_f32 v24, v36, v37
	v_cvt_pk_fp8_f32 v25, v40, v41
	v_cvt_pk_fp8_f32 v26, v44, v45
	v_cvt_pk_fp8_f32 v27, v48, v49
	v_pk_mul_f32 v[34:35], v[34:35], v[50:51] op_sel_hi:[1,0]
	v_pk_mul_f32 v[38:39], v[38:39], v[50:51] op_sel_hi:[1,0]
	v_pk_mul_f32 v[42:43], v[42:43], v[50:51] op_sel_hi:[1,0]
	v_pk_mul_f32 v[46:47], v[46:47], v[50:51] op_sel_hi:[1,0]
	v_cvt_pk_fp8_f32 v24, v34, v35 op_sel:[0,0,1]
	v_cvt_pk_fp8_f32 v25, v38, v39 op_sel:[0,0,1]
	v_cvt_pk_fp8_f32 v26, v42, v43 op_sel:[0,0,1]
	v_cvt_pk_fp8_f32 v27, v46, v47 op_sel:[0,0,1]
	global_store_dwordx2 v[28:29], v[24:25], off
	global_store_dwordx2 v[28:29], v[26:27], off offset:128
	v_pk_fma_f32 v[36:37], v[162:163], s[14:15], v[14:15] op_sel_hi:[1,0,1]
	v_pk_fma_f32 v[40:41], v[158:159], s[14:15], v[10:11] op_sel_hi:[1,0,1]
	v_mov_b32_e32 v24, 0
	v_mov_b32_e32 v25, 0
	v_pk_fma_f32 v[44:45], v[154:155], s[14:15], v[6:7] op_sel_hi:[1,0,1]
	v_pk_fma_f32 v[48:49], v[150:151], s[14:15], v[2:3] op_sel_hi:[1,0,1]
	v_mov_b32_e32 v26, 0
	v_mov_b32_e32 v27, 0
	v_pk_fma_f32 v[34:35], v[164:165], s[14:15], v[16:17] op_sel_hi:[1,0,1]
	v_pk_fma_f32 v[38:39], v[160:161], s[14:15], v[12:13] op_sel_hi:[1,0,1]
	v_pk_fma_f32 v[42:43], v[156:157], s[14:15], v[8:9] op_sel_hi:[1,0,1]
	v_pk_fma_f32 v[46:47], v[152:153], s[14:15], v[4:5] op_sel_hi:[1,0,1]
	v_add_u32_e32 v28, 48, v20
	v_ashrrev_i32_e32 v29, 31, v28
	v_sub_co_u32_e32 v32, vcc, v28, v22
	v_mul_f32_e32 v50, 0x42000000, v227
	v_pk_mul_f32 v[36:37], v[36:37], v[50:51] op_sel_hi:[1,0]
	v_pk_mul_f32 v[40:41], v[40:41], v[50:51] op_sel_hi:[1,0]
	v_pk_mul_f32 v[44:45], v[44:45], v[50:51] op_sel_hi:[1,0]
	v_pk_mul_f32 v[48:49], v[48:49], v[50:51] op_sel_hi:[1,0]
	v_cvt_pk_fp8_f32 v24, v36, v37
	v_cvt_pk_fp8_f32 v25, v40, v41
	v_cvt_pk_fp8_f32 v26, v44, v45
	v_cvt_pk_fp8_f32 v27, v48, v49
	v_pk_mul_f32 v[34:35], v[34:35], v[50:51] op_sel_hi:[1,0]
	v_pk_mul_f32 v[38:39], v[38:39], v[50:51] op_sel_hi:[1,0]
	v_pk_mul_f32 v[42:43], v[42:43], v[50:51] op_sel_hi:[1,0]
	v_pk_mul_f32 v[46:47], v[46:47], v[50:51] op_sel_hi:[1,0]
	v_cvt_pk_fp8_f32 v24, v34, v35 op_sel:[0,0,1]
	v_cvt_pk_fp8_f32 v25, v38, v39 op_sel:[0,0,1]
	v_cvt_pk_fp8_f32 v26, v42, v43 op_sel:[0,0,1]
	v_cvt_pk_fp8_f32 v27, v46, v47 op_sel:[0,0,1]
	v_subb_co_u32_e32 v33, vcc, v29, v23, vcc
	v_lshl_add_u64 v[32:33], v[32:33], 2, s[30:31]
	global_store_dwordx2 v[30:31], v[24:25], off
	global_store_dwordx2 v[30:31], v[26:27], off offset:128
	v_pk_fma_f32 v[32:33], v[146:147], s[14:15], v[14:15] op_sel_hi:[1,0,1]
	v_pk_fma_f32 v[36:37], v[142:143], s[14:15], v[10:11] op_sel_hi:[1,0,1]
	v_mov_b32_e32 v24, 0
	v_mov_b32_e32 v25, 0
	v_pk_fma_f32 v[40:41], v[138:139], s[14:15], v[6:7] op_sel_hi:[1,0,1]
	v_pk_fma_f32 v[44:45], v[134:135], s[14:15], v[2:3] op_sel_hi:[1,0,1]
	v_mov_b32_e32 v26, 0
	v_mov_b32_e32 v27, 0
	v_pk_fma_f32 v[30:31], v[148:149], s[14:15], v[16:17] op_sel_hi:[1,0,1]
	v_pk_fma_f32 v[34:35], v[144:145], s[14:15], v[12:13] op_sel_hi:[1,0,1]
	v_pk_fma_f32 v[38:39], v[140:141], s[14:15], v[8:9] op_sel_hi:[1,0,1]
	v_pk_fma_f32 v[42:43], v[136:137], s[14:15], v[4:5] op_sel_hi:[1,0,1]
	v_lshlrev_b64 v[28:29], 11, v[28:29]
	v_lshl_add_u64 v[28:29], s[6:7], 0, v[28:29]
	s_and_b64 vcc, exec, s[2:3]
	v_lshl_add_u64 v[28:29], v[28:29], 0, v[18:19]
	v_mul_f32_e32 v46, 0x42000000, v228
	v_pk_mul_f32 v[32:33], v[32:33], v[46:47] op_sel_hi:[1,0]
	v_pk_mul_f32 v[36:37], v[36:37], v[46:47] op_sel_hi:[1,0]
	v_pk_mul_f32 v[40:41], v[40:41], v[46:47] op_sel_hi:[1,0]
	v_pk_mul_f32 v[44:45], v[44:45], v[46:47] op_sel_hi:[1,0]
	v_cvt_pk_fp8_f32 v24, v32, v33
	v_cvt_pk_fp8_f32 v25, v36, v37
	v_cvt_pk_fp8_f32 v26, v40, v41
	v_cvt_pk_fp8_f32 v27, v44, v45
	v_pk_mul_f32 v[30:31], v[30:31], v[46:47] op_sel_hi:[1,0]
	v_pk_mul_f32 v[34:35], v[34:35], v[46:47] op_sel_hi:[1,0]
	v_pk_mul_f32 v[38:39], v[38:39], v[46:47] op_sel_hi:[1,0]
	v_pk_mul_f32 v[42:43], v[42:43], v[46:47] op_sel_hi:[1,0]
	v_cvt_pk_fp8_f32 v24, v30, v31 op_sel:[0,0,1]
	v_cvt_pk_fp8_f32 v25, v34, v35 op_sel:[0,0,1]
	v_cvt_pk_fp8_f32 v26, v38, v39 op_sel:[0,0,1]
	v_cvt_pk_fp8_f32 v27, v42, v43 op_sel:[0,0,1]
	global_store_dwordx2 v[28:29], v[24:25], off
	global_store_dwordx2 v[28:29], v[26:27], off offset:128
	s_cbranch_vccz .LBB0_1478
	s_andn2_b64 vcc, exec, s[26:27]
	s_mov_b64 s[2:3], -1
	s_cbranch_vccnz .LBB0_1457
	s_branch .LBB0_1479

; __device__ __forceinline__ unsigned pack_fp8x4(float a, float b, float c, float d) { int w = __builtin_amdgcn_cvt_pk_fp8_f32(a, b, 0, false); w = __builtin_amdgcn_cvt_pk_fp8_f32(c, d, w, true); return (unsigned)w; }
;     __device__ __forceinline__ void operator()(const f32x4 (&acc)[2][2][4][2], const Unit& u, int wr, int wc, int fr, int fq) const {
;     ...
;         for (int ai = 0; ai < 2; ++ai) if (!(ai == 1 && u.half))
; #pragma unroll
;             for (int m = 0; m < 4; ++m) { const size_t row = (size_t)(row0 + ai * HALF + m * 16); const float sw = 32.f * SWE[(size_t)e * 8192 + (row - (size_t)eoff0)];
; #pragma unroll
;                 for (int bj = 0; bj < 2; ++bj) { const f32x4 v0 = (acc[ai][bj][m][0] * 0.015625f + bv[bj][0]) * sw, v1 = (acc[ai][bj][m][1] * 0.015625f + bv[bj][1]) * sw;
;                     uint2 w; w.x = pack_fp8x4(v0[0], v0[1], v0[2], v0[3]); w.y = pack_fp8x4(v1[0], v1[1], v1[2], v1[3]);
;                     *(uint2*)(YS + row * 2048 + col0 + bj * HALF) = w; } }
.LBB0_1478:
	v_add_u32_e32 v24, 0x80, v20
	v_ashrrev_i32_e32 v25, 31, v24
	v_sub_co_u32_e32 v26, vcc, v24, v22
	v_pk_fma_f32 v[28:29], v[130:131], s[14:15], v[14:15] op_sel_hi:[1,0,1]
	s_nop 0
	v_subb_co_u32_e32 v27, vcc, v25, v23, vcc
	v_lshl_add_u64 v[26:27], v[26:27], 2, s[30:31]
	v_pk_fma_f32 v[32:33], v[126:127], s[14:15], v[10:11] op_sel_hi:[1,0,1]
	v_mov_b32_e32 v34, v66
	v_mov_b32_e32 v35, v66
	v_pk_fma_f32 v[38:39], v[122:123], s[14:15], v[6:7] op_sel_hi:[1,0,1]
	v_pk_fma_f32 v[42:43], v[118:119], s[14:15], v[2:3] op_sel_hi:[1,0,1]
	v_mov_b32_e32 v44, v66
	v_mov_b32_e32 v45, v66
	v_pk_fma_f32 v[26:27], v[132:133], s[14:15], v[16:17] op_sel_hi:[1,0,1]
	v_pk_fma_f32 v[30:31], v[128:129], s[14:15], v[12:13] op_sel_hi:[1,0,1]
	v_pk_fma_f32 v[36:37], v[124:125], s[14:15], v[8:9] op_sel_hi:[1,0,1]
	v_pk_fma_f32 v[40:41], v[120:121], s[14:15], v[4:5] op_sel_hi:[1,0,1]
	v_add_u32_e32 v46, 0x90, v20
	v_lshlrev_b64 v[24:25], 11, v[24:25]
	v_ashrrev_i32_e32 v47, 31, v46
	v_sub_co_u32_e32 v48, vcc, v46, v22
	v_lshl_add_u64 v[24:25], s[6:7], 0, v[24:25]
	s_nop 0
	v_subb_co_u32_e32 v49, vcc, v47, v23, vcc
	v_lshl_add_u64 v[24:25], v[24:25], 0, v[18:19]
	v_lshlrev_b64 v[46:47], 11, v[46:47]
	v_lshl_add_u64 v[46:47], s[6:7], 0, v[46:47]
	v_mul_f32_e32 v50, 0x42000000, v229
	v_pk_mul_f32 v[28:29], v[28:29], v[50:51] op_sel_hi:[1,0]
	v_pk_mul_f32 v[32:33], v[32:33], v[50:51] op_sel_hi:[1,0]
	v_pk_mul_f32 v[38:39], v[38:39], v[50:51] op_sel_hi:[1,0]
	v_pk_mul_f32 v[42:43], v[42:43], v[50:51] op_sel_hi:[1,0]
	v_cvt_pk_fp8_f32 v34, v28, v29
	v_cvt_pk_fp8_f32 v35, v32, v33
	v_cvt_pk_fp8_f32 v44, v38, v39
	v_cvt_pk_fp8_f32 v45, v42, v43
	v_pk_mul_f32 v[26:27], v[26:27], v[50:51] op_sel_hi:[1,0]
	v_pk_mul_f32 v[30:31], v[30:31], v[50:51] op_sel_hi:[1,0]
	v_pk_mul_f32 v[36:37], v[36:37], v[50:51] op_sel_hi:[1,0]
	v_pk_mul_f32 v[40:41], v[40:41], v[50:51] op_sel_hi:[1,0]
	v_cvt_pk_fp8_f32 v34, v26, v27 op_sel:[0,0,1]
	v_cvt_pk_fp8_f32 v35, v30, v31 op_sel:[0,0,1]
	v_cvt_pk_fp8_f32 v44, v36, v37 op_sel:[0,0,1]
	v_cvt_pk_fp8_f32 v45, v40, v41 op_sel:[0,0,1]
	v_lshl_add_u64 v[26:27], v[48:49], 2, s[30:31]
	global_store_dwordx2 v[24:25], v[34:35], off
	global_store_dwordx2 v[24:25], v[44:45], off offset:128
	v_pk_fma_f32 v[26:27], v[114:115], s[14:15], v[14:15] op_sel_hi:[1,0,1]
	v_pk_fma_f32 v[30:31], v[110:111], s[14:15], v[10:11] op_sel_hi:[1,0,1]
	v_mov_b32_e32 v32, v66
	v_mov_b32_e32 v33, v66
	v_pk_fma_f32 v[36:37], v[106:107], s[14:15], v[6:7] op_sel_hi:[1,0,1]
	v_pk_fma_f32 v[40:41], v[102:103], s[14:15], v[2:3] op_sel_hi:[1,0,1]
	v_mov_b32_e32 v42, v66
	v_mov_b32_e32 v43, v66
	v_pk_fma_f32 v[24:25], v[116:117], s[14:15], v[16:17] op_sel_hi:[1,0,1]
	v_pk_fma_f32 v[28:29], v[112:113], s[14:15], v[12:13] op_sel_hi:[1,0,1]
	v_pk_fma_f32 v[34:35], v[108:109], s[14:15], v[8:9] op_sel_hi:[1,0,1]
	v_pk_fma_f32 v[38:39], v[104:105], s[14:15], v[4:5] op_sel_hi:[1,0,1]
	v_add_u32_e32 v44, 0xa0, v20
	v_ashrrev_i32_e32 v45, 31, v44
	v_sub_co_u32_e32 v48, vcc, v44, v22
	v_add_u32_e32 v20, 0xb0, v20
	s_nop 0
	v_subb_co_u32_e32 v49, vcc, v45, v23, vcc
	v_lshlrev_b64 v[44:45], 11, v[44:45]
	v_sub_co_u32_e32 v22, vcc, v20, v22
	v_lshl_add_u64 v[44:45], s[6:7], 0, v[44:45]
	v_mul_f32_e32 v50, 0x42000000, v230
	v_pk_mul_f32 v[26:27], v[26:27], v[50:51] op_sel_hi:[1,0]
	v_pk_mul_f32 v[30:31], v[30:31], v[50:51] op_sel_hi:[1,0]
	v_pk_mul_f32 v[36:37], v[36:37], v[50:51] op_sel_hi:[1,0]
	v_pk_mul_f32 v[40:41], v[40:41], v[50:51] op_sel_hi:[1,0]
	v_cvt_pk_fp8_f32 v32, v26, v27
	v_cvt_pk_fp8_f32 v33, v30, v31
	v_cvt_pk_fp8_f32 v42, v36, v37
	v_cvt_pk_fp8_f32 v43, v40, v41
	v_pk_mul_f32 v[24:25], v[24:25], v[50:51] op_sel_hi:[1,0]
	v_pk_mul_f32 v[28:29], v[28:29], v[50:51] op_sel_hi:[1,0]
	v_pk_mul_f32 v[34:35], v[34:35], v[50:51] op_sel_hi:[1,0]
	v_pk_mul_f32 v[38:39], v[38:39], v[50:51] op_sel_hi:[1,0]
	v_cvt_pk_fp8_f32 v32, v24, v25 op_sel:[0,0,1]
; __device__ __forceinline__ unsigned pack_fp8x4(float a, float b, float c, float d) { int w = __builtin_amdgcn_cvt_pk_fp8_f32(a, b, 0, false); w = __builtin_amdgcn_cvt_pk_fp8_f32(c, d, w, true); return (unsigned)w; }
;     __device__ __forceinline__ void operator()(const f32x4 (&acc)[2][2][4][2], const Unit& u, int wr, int wc, int fr, int fq) const {
;     ...
;             for (int m = 0; m < 4; ++m) { const size_t row = (size_t)(row0 + ai * HALF + m * 16); const float sw = 32.f * SWE[(size_t)e * 8192 + (row - (size_t)eoff0)];
; #pragma unroll
;                 for (int bj = 0; bj < 2; ++bj) { const f32x4 v0 = (acc[ai][bj][m][0] * 0.015625f + bv[bj][0]) * sw, v1 = (acc[ai][bj][m][1] * 0.015625f + bv[bj][1]) * sw;
;                     uint2 w; w.x = pack_fp8x4(v0[0], v0[1], v0[2], v0[3]); w.y = pack_fp8x4(v1[0], v1[1], v1[2], v1[3]);
;                     *(uint2*)(YS + row * 2048 + col0 + bj * HALF) = w; } }
	v_cvt_pk_fp8_f32 v33, v28, v29 op_sel:[0,0,1]
	v_cvt_pk_fp8_f32 v42, v34, v35 op_sel:[0,0,1]
	v_cvt_pk_fp8_f32 v43, v38, v39 op_sel:[0,0,1]
	v_lshl_add_u64 v[26:27], v[46:47], 0, v[18:19]
	v_lshl_add_u64 v[24:25], v[48:49], 2, s[30:31]
	global_store_dwordx2 v[26:27], v[32:33], off
	global_store_dwordx2 v[26:27], v[42:43], off offset:128
	v_pk_fma_f32 v[26:27], v[98:99], s[14:15], v[14:15] op_sel_hi:[1,0,1]
	v_pk_fma_f32 v[30:31], v[94:95], s[14:15], v[10:11] op_sel_hi:[1,0,1]
	v_mov_b32_e32 v32, v66
	v_mov_b32_e32 v33, v66
	v_pk_fma_f32 v[36:37], v[90:91], s[14:15], v[6:7] op_sel_hi:[1,0,1]
	v_pk_fma_f32 v[40:41], v[86:87], s[14:15], v[2:3] op_sel_hi:[1,0,1]
	v_mov_b32_e32 v42, v66
	v_mov_b32_e32 v43, v66
	v_pk_fma_f32 v[24:25], v[100:101], s[14:15], v[16:17] op_sel_hi:[1,0,1]
	v_pk_fma_f32 v[28:29], v[96:97], s[14:15], v[12:13] op_sel_hi:[1,0,1]
	v_pk_fma_f32 v[34:35], v[92:93], s[14:15], v[8:9] op_sel_hi:[1,0,1]
	v_pk_fma_f32 v[38:39], v[88:89], s[14:15], v[4:5] op_sel_hi:[1,0,1]
	v_ashrrev_i32_e32 v21, 31, v20
	v_subb_co_u32_e32 v23, vcc, v21, v23, vcc
	v_lshl_add_u64 v[22:23], v[22:23], 2, s[30:31]
	v_pk_fma_f32 v[14:15], v[82:83], s[14:15], v[14:15] op_sel_hi:[1,0,1]
	v_pk_fma_f32 v[10:11], v[78:79], s[14:15], v[10:11] op_sel_hi:[1,0,1]
	v_pk_fma_f32 v[6:7], v[74:75], s[14:15], v[6:7] op_sel_hi:[1,0,1]
	v_pk_fma_f32 v[2:3], v[70:71], s[14:15], v[2:3] op_sel_hi:[1,0,1]
	v_pk_fma_f32 v[16:17], v[84:85], s[14:15], v[16:17] op_sel_hi:[1,0,1]
	v_pk_fma_f32 v[12:13], v[80:81], s[14:15], v[12:13] op_sel_hi:[1,0,1]
	v_pk_fma_f32 v[8:9], v[76:77], s[14:15], v[8:9] op_sel_hi:[1,0,1]
	v_pk_fma_f32 v[4:5], v[72:73], s[14:15], v[4:5] op_sel_hi:[1,0,1]
	v_lshlrev_b64 v[20:21], 11, v[20:21]
	v_mul_f32_e32 v46, 0x42000000, v231
	v_pk_mul_f32 v[26:27], v[26:27], v[46:47] op_sel_hi:[1,0]
	v_pk_mul_f32 v[30:31], v[30:31], v[46:47] op_sel_hi:[1,0]
	v_pk_mul_f32 v[36:37], v[36:37], v[46:47] op_sel_hi:[1,0]
	v_pk_mul_f32 v[40:41], v[40:41], v[46:47] op_sel_hi:[1,0]
	v_cvt_pk_fp8_f32 v32, v26, v27
	v_cvt_pk_fp8_f32 v33, v30, v31
	v_cvt_pk_fp8_f32 v42, v36, v37
	v_cvt_pk_fp8_f32 v43, v40, v41
	v_pk_mul_f32 v[24:25], v[24:25], v[46:47] op_sel_hi:[1,0]
	v_pk_mul_f32 v[28:29], v[28:29], v[46:47] op_sel_hi:[1,0]
	v_pk_mul_f32 v[34:35], v[34:35], v[46:47] op_sel_hi:[1,0]
	v_pk_mul_f32 v[38:39], v[38:39], v[46:47] op_sel_hi:[1,0]
	v_cvt_pk_fp8_f32 v32, v24, v25 op_sel:[0,0,1]
	v_cvt_pk_fp8_f32 v33, v28, v29 op_sel:[0,0,1]
	v_cvt_pk_fp8_f32 v42, v34, v35 op_sel:[0,0,1]
	v_cvt_pk_fp8_f32 v43, v38, v39 op_sel:[0,0,1]
	v_lshl_add_u64 v[24:25], v[44:45], 0, v[18:19]
	global_store_dwordx2 v[24:25], v[32:33], off
	global_store_dwordx2 v[24:25], v[42:43], off offset:128
	v_mov_b32_e32 v22, v66
	v_mov_b32_e32 v23, v66
	v_mov_b32_e32 v24, v66
	v_mov_b32_e32 v25, v66
	v_mul_f32_e32 v26, 0x42000000, v232
	v_pk_mul_f32 v[14:15], v[14:15], v[26:27] op_sel_hi:[1,0]
	v_pk_mul_f32 v[10:11], v[10:11], v[26:27] op_sel_hi:[1,0]
	v_pk_mul_f32 v[6:7], v[6:7], v[26:27] op_sel_hi:[1,0]
	v_pk_mul_f32 v[2:3], v[2:3], v[26:27] op_sel_hi:[1,0]
	v_cvt_pk_fp8_f32 v22, v14, v15
	v_cvt_pk_fp8_f32 v23, v10, v11
	v_cvt_pk_fp8_f32 v24, v6, v7
	v_cvt_pk_fp8_f32 v25, v2, v3
	v_pk_mul_f32 v[16:17], v[16:17], v[26:27] op_sel_hi:[1,0]
	v_pk_mul_f32 v[12:13], v[12:13], v[26:27] op_sel_hi:[1,0]
	v_pk_mul_f32 v[8:9], v[8:9], v[26:27] op_sel_hi:[1,0]
	v_pk_mul_f32 v[4:5], v[4:5], v[26:27] op_sel_hi:[1,0]
	v_cvt_pk_fp8_f32 v22, v16, v17 op_sel:[0,0,1]
	v_cvt_pk_fp8_f32 v23, v12, v13 op_sel:[0,0,1]
	v_cvt_pk_fp8_f32 v24, v8, v9 op_sel:[0,0,1]
	v_cvt_pk_fp8_f32 v25, v4, v5 op_sel:[0,0,1]
	v_lshl_add_u64 v[2:3], s[6:7], 0, v[20:21]
	v_lshl_add_u64 v[2:3], v[2:3], 0, v[18:19]
	global_store_dwordx2 v[2:3], v[22:23], off
	global_store_dwordx2 v[2:3], v[24:25], off offset:128
	s_andn2_b64 vcc, exec, s[26:27]
	s_mov_b64 s[2:3], -1
	s_cbranch_vccnz .LBB0_1457
